# speedup vs baseline: 1.0095x; 1.0095x over previous
_Z11proj_kernelPKfS0_S0_PKDF16_S0_S0_S0_PDF16_S3_S3_Pj:
	s_ashr_i32 s12, s2, 6
	s_load_dwordx8 s[4:11], s[0:1], 0x0
	s_cmp_gt_u32 s2, 63
	s_cselect_b64 s[22:23], -1, 0
	s_cmp_lg_u32 s12, 1
	s_cselect_b64 s[18:19], -1, 0
	s_cmp_eq_u32 s12, 1
	s_cselect_b64 s[20:21], -1, 0
	s_and_b64 s[14:15], s[20:21], exec
	s_waitcnt lgkmcnt(0)
	s_cselect_b32 s14, s6, s8
	s_cselect_b32 s15, s7, s9
	s_ashr_i32 s13, s12, 31
	s_lshl_b32 s28, s2, 7
	s_lshl_b64 s[6:7], s[12:13], 19
	s_and_b32 s3, s28, 0x1f80
	s_cmp_lt_u32 s2, 64
	s_cselect_b64 vcc, -1, 0
	v_lshrrev_b32_e32 v1, 2, v0
	v_lshrrev_b32_e32 v2, 2, v0
	v_and_b32_e32 v2, 0x70, v2
	v_bfe_u32 v254, v0, 3, 3
	v_or_b32_e32 v254, v2, v254
	v_or_b32_e32 v2, s3, v254
	s_and_b64 s[8:9], vcc, exec
	s_cselect_b32 s25, s5, s15
	s_cselect_b32 s24, s4, s14
	v_lshlrev_b32_e32 v2, 11, v2
	v_mov_b32_e32 v3, 0
	v_lshlrev_b32_e32 v6, 4, v0
	s_add_u32 s4, s10, s6
	v_lshl_add_u64 v[4:5], s[24:25], 0, v[2:3]
	v_and_b32_e32 v6, 0x70, v6
	v_mov_b32_e32 v7, v3
	v_lshlrev_b32_e32 v56, 4, v0
	v_mov_b32_e32 v57, v3
	s_addc_u32 s5, s11, s7
	v_lshl_add_u64 v[4:5], v[4:5], 0, v[6:7]
	s_mov_b64 s[46:47], 0x4000
	v_lshl_add_u64 v[250:251], v[4:5], 0, s[46:47]
	s_movk_i32 s8, 0x2000
	v_lshl_add_u64 v[6:7], s[4:5], 0, v[56:57]
	global_load_dwordx4 v[8:11], v[4:5], off sc1 nt
	global_load_dwordx4 v[12:15], v[250:251], off sc1 nt
	global_load_dwordx4 v[16:19], v56, s[4:5] sc1
	v_add_co_u32_e64 v28, s[4:5], s8, v6
	s_mov_b32 s33, 0xa000
	s_nop 0
	v_addc_co_u32_e64 v29, s[4:5], 0, v7, s[4:5]
	s_movk_i32 s4, 0x4000
	s_nop 0
	v_add_co_u32_e64 v30, s[4:5], s4, v6
	s_mov_b32 s6, 0xe000
	s_nop 0
	v_addc_co_u32_e64 v31, s[4:5], 0, v7, s[4:5]
	global_load_dwordx4 v[20:23], v[28:29], off sc1
	global_load_dwordx4 v[24:27], v[30:31], off sc1
	s_movk_i32 s4, 0x6000
	v_add_co_u32_e64 v40, s[4:5], s4, v6
	v_lshlrev_b32_e32 v57, 6, v1
	s_nop 0
	v_addc_co_u32_e64 v41, s[4:5], 0, v7, s[4:5]
	global_load_dwordx4 v[28:31], v[40:41], off sc1
	global_load_dwordx4 v[32:35], v[4:5], off offset:128 sc1 nt
	global_load_dwordx4 v[36:39], v[250:251], off offset:128 sc1 nt
	s_mov_b32 s4, 0x8000
	v_add_co_u32_e64 v40, s[4:5], s4, v6
	v_bitop3_b32 v58, v56, 48, v0 bitop3:0x48
	s_nop 0
	v_addc_co_u32_e64 v41, s[4:5], 0, v7, s[4:5]
	v_add_co_u32_e64 v44, s[4:5], s33, v6
	global_load_dwordx4 v[40:43], v[40:41], off sc1
	s_nop 0
	v_addc_co_u32_e64 v45, s[4:5], 0, v7, s[4:5]
	s_mov_b32 s4, 0xc000
	s_nop 0
	v_add_co_u32_e64 v48, s[4:5], s4, v6
	global_load_dwordx4 v[44:47], v[44:45], off sc1
	s_nop 0
	v_addc_co_u32_e64 v49, s[4:5], 0, v7, s[4:5]
	v_add_co_u32_e64 v52, s[4:5], s6, v6
	global_load_dwordx4 v[48:51], v[48:49], off sc1
	s_nop 0
	v_addc_co_u32_e64 v53, s[4:5], 0, v7, s[4:5]
	global_load_dwordx4 v[52:55], v[52:53], off sc1
	s_mov_b32 s4, 0x1e000
	v_bfe_u32 v57, v0, 1, 2
	v_bfe_u32 v58, v254, 2, 2
	v_xor_b32_e32 v57, v57, v58
	v_lshlrev_b32_e32 v57, 4, v57
	v_and_b32_e32 v58, 1, v0
	v_lshl_or_b32 v57, v58, 3, v57
	v_lshl_add_u32 v209, v254, 6, v57
	v_xor_b32_e32 v248, 32, v209
	v_add_u32_e32 v248, 0x200, v248
	v_add_u32_e32 v208, 0, v56
	v_readfirstlane_b32 s30, v0
	v_bfe_u32 v207, v0, 5, 1
	v_bitop3_b32 v1, v207, v1, 3 bitop3:0x78
	v_lshlrev_b32_e32 v210, 4, v1
	s_mov_b32 s34, 0x14000
	v_add_u32_e32 v213, 0x2000, v208
	s_mov_b32 s43, 0
	s_lshr_b32 s29, s30, 6
	s_mov_b32 s35, -2
	s_mov_b32 s36, 0xffff2000
	s_mov_b32 s37, 0xffff4000
	s_mov_b32 s38, 0xffff6000
	s_movk_i32 s39, 0x8000
	s_movk_i32 s40, 0xa000
	s_movk_i32 s41, 0xc000
	s_movk_i32 s42, 0xe000
	s_mov_b64 s[26:27], 0x100
	v_mov_b32_e32 v56, v3
	v_mov_b32_e32 v57, v3
	v_mov_b32_e32 v58, v3
	v_mov_b32_e32 v59, v3
	v_mov_b32_e32 v60, v3
	v_mov_b32_e32 v61, v3
	v_mov_b32_e32 v62, v3
	v_mov_b32_e32 v63, v3
	v_mov_b32_e32 v64, v3
	v_mov_b32_e32 v65, v3
	v_mov_b32_e32 v66, v3
	v_mov_b32_e32 v67, v3
	v_mov_b32_e32 v68, v3
	v_mov_b32_e32 v69, v3
	v_mov_b32_e32 v70, v3
	v_mov_b32_e32 v71, v3
	v_mov_b32_e32 v72, v3
	v_mov_b32_e32 v73, v3
	v_mov_b32_e32 v74, v3
	v_mov_b32_e32 v75, v3
	v_mov_b32_e32 v76, v3
	v_mov_b32_e32 v77, v3
	v_mov_b32_e32 v78, v3
	v_mov_b32_e32 v79, v3
	v_mov_b32_e32 v80, v3
	v_mov_b32_e32 v81, v3
	v_mov_b32_e32 v82, v3
	v_mov_b32_e32 v83, v3
	v_mov_b32_e32 v84, v3
	v_mov_b32_e32 v85, v3
	v_mov_b32_e32 v86, v3
	v_mov_b32_e32 v87, v3
	v_mov_b32_e32 v88, v3
	v_mov_b32_e32 v89, v3
	v_mov_b32_e32 v90, v3
	v_mov_b32_e32 v91, v3
	v_mov_b32_e32 v92, v3
	v_mov_b32_e32 v93, v3
	v_mov_b32_e32 v94, v3
	v_mov_b32_e32 v95, v3
	v_mov_b32_e32 v96, v3
	v_mov_b32_e32 v97, v3
	v_mov_b32_e32 v98, v3
	v_mov_b32_e32 v99, v3
	v_mov_b32_e32 v100, v3
	v_mov_b32_e32 v101, v3
	v_mov_b32_e32 v102, v3
	v_mov_b32_e32 v103, v3
	v_mov_b32_e32 v104, v3
	v_mov_b32_e32 v105, v3
	v_mov_b32_e32 v106, v3
	v_mov_b32_e32 v107, v3
	v_mov_b32_e32 v108, v3
	v_mov_b32_e32 v109, v3
	v_mov_b32_e32 v110, v3
	v_mov_b32_e32 v111, v3
	v_mov_b32_e32 v112, v3
	v_mov_b32_e32 v113, v3
	v_mov_b32_e32 v114, v3
	v_mov_b32_e32 v115, v3
	v_mov_b32_e32 v116, v3
	v_mov_b32_e32 v117, v3
	v_mov_b32_e32 v118, v3
	v_mov_b32_e32 v119, v3
	v_mov_b32_e32 v120, v3
	v_mov_b32_e32 v121, v3
	v_mov_b32_e32 v122, v3
	v_mov_b32_e32 v123, v3
	v_mov_b32_e32 v124, v3
	v_mov_b32_e32 v125, v3
	v_mov_b32_e32 v126, v3
	v_mov_b32_e32 v127, v3
	v_mov_b32_e32 v128, v3
	v_mov_b32_e32 v129, v3
	s_waitcnt vmcnt(11)
	v_cvt_pk_f16_f32 v8, v8, v9
	v_cvt_pk_f16_f32 v9, v10, v11
	s_waitcnt vmcnt(10)
	v_cvt_pk_f16_f32 v10, v12, v13
	v_cvt_pk_f16_f32 v11, v14, v15
	ds_write_b64 v209, v[8:9]
	ds_write_b64 v248, v[10:11]
	v_and_b32_e32 v10, 31, v0
	s_waitcnt vmcnt(9)
	ds_write_b128 v208, v[16:19] offset:8192
	s_waitcnt vmcnt(8)
	ds_write_b128 v208, v[20:23] offset:16384
	s_waitcnt vmcnt(7)
	ds_write_b128 v208, v[24:27] offset:24576
	s_load_dwordx2 s[16:17], s[0:1], 0x50
	s_load_dwordx4 s[12:15], s[0:1], 0x40
	s_load_dwordx8 s[4:11], s[0:1], 0x20
	s_lshl_b32 s0, s30, 1
	s_and_b32 s31, s0, 0x180
	s_lshr_b32 s0, s30, 2
	v_bfe_u32 v11, v0, 2, 2
	s_and_b32 s0, s0, 0x3fffffc0
	s_waitcnt vmcnt(5)
	v_cvt_pk_f16_f32 v8, v32, v33
	v_cvt_pk_f16_f32 v9, v34, v35
	v_or_b32_e32 v12, s31, v10
	v_or_b32_e32 v206, s0, v10
	v_bitop3_b32 v1, v207, v11, 2 bitop3:0x36
	s_waitcnt vmcnt(4)
	v_cvt_pk_f16_f32 v10, v36, v37
	v_cvt_pk_f16_f32 v11, v38, v39
	s_mov_b32 s0, 0x10000
	ds_write_b128 v208, v[28:31] offset:32768
	ds_write_b64 v209, v[8:9] offset:40960
	ds_write_b64 v248, v[10:11] offset:40960
	v_add_co_u32_e64 v8, s[0:1], s0, v6
	global_load_dwordx4 v[154:157], v[250:251], off offset:256 sc1 nt
	global_load_dwordx4 v[162:165], v[4:5], off offset:256 sc1 nt
	v_addc_co_u32_e64 v9, s[0:1], 0, v7, s[0:1]
	s_mov_b32 s0, 0x12000
	global_load_dwordx4 v[158:161], v[8:9], off sc1
	v_add_co_u32_e64 v8, s[0:1], s0, v6
	v_lshl_add_u32 v211, v12, 6, 0
	s_nop 0
	v_addc_co_u32_e64 v9, s[0:1], 0, v7, s[0:1]
	v_add_co_u32_e64 v10, s[0:1], s34, v6
	v_add_u32_e32 v14, 0x12000, v208
	s_nop 0
	v_addc_co_u32_e64 v11, s[0:1], 0, v7, s[0:1]
	s_mov_b32 s0, 0x16000
	s_nop 0
	v_add_co_u32_e64 v12, s[0:1], s0, v6
	s_waitcnt vmcnt(3)
	ds_write_b128 v14, v[52:55]
	v_addc_co_u32_e64 v13, s[0:1], 0, v7, s[0:1]
	s_mov_b32 s0, 0x18000
	s_nop 0
	v_add_co_u32_e64 v14, s[0:1], s0, v6
	ds_write_b128 v208, v[40:43] offset:49152
	s_nop 0
	v_addc_co_u32_e64 v15, s[0:1], 0, v7, s[0:1]
	s_mov_b32 s0, 0x1a000
	s_nop 0
	v_add_co_u32_e64 v16, s[0:1], s0, v6
	ds_write_b128 v208, v[44:47] offset:57344
	s_nop 0
	v_addc_co_u32_e64 v17, s[0:1], 0, v7, s[0:1]
	s_mov_b32 s0, 0x1c000
	ds_write_b128 v213, v[48:51] offset:57344
	v_mov_b32_e32 v21, v3
	v_mov_b32_e32 v22, v3
	v_mov_b32_e32 v23, v3
	v_mov_b32_e32 v24, v3
	v_mov_b32_e32 v25, v3
	v_mov_b32_e32 v26, v3
	v_mov_b32_e32 v27, v3
	v_mov_b32_e32 v28, v3
	v_mov_b32_e32 v29, v3
	v_mov_b32_e32 v30, v3
	v_mov_b32_e32 v31, v3
	v_mov_b32_e32 v32, v3
	v_mov_b32_e32 v33, v3
	v_mov_b32_e32 v34, v3
	v_mov_b32_e32 v35, v3
	v_mov_b32_e32 v36, v3
	v_mov_b32_e32 v37, v3
	v_mov_b32_e32 v38, v3
	v_mov_b32_e32 v39, v3
	v_mov_b32_e32 v40, v3
	v_mov_b32_e32 v41, v3
	v_mov_b32_e32 v42, v3
	v_mov_b32_e32 v43, v3
	v_mov_b32_e32 v44, v3
	v_mov_b32_e32 v45, v3
	v_mov_b32_e32 v46, v3
	v_mov_b32_e32 v47, v3
	v_mov_b32_e32 v48, v3
	v_mov_b32_e32 v49, v3
	v_mov_b32_e32 v50, v3
	v_mov_b32_e32 v51, v3
	v_mov_b32_e32 v52, v3
	v_mov_b32_e32 v53, v3
	v_mov_b32_e32 v54, v3
	v_mov_b32_e32 v55, v3
	v_add_co_u32_e64 v18, s[0:1], s0, v6
	v_add_u32_e32 v216, v211, v210
	s_nop 0
	v_addc_co_u32_e64 v19, s[0:1], 0, v7, s[0:1]
	global_load_dwordx4 v[174:177], v[8:9], off sc1
	global_load_dwordx4 v[166:169], v[10:11], off sc1
	global_load_dwordx4 v[170:173], v[12:13], off sc1
	global_load_dwordx4 v[142:145], v[250:251], off offset:384 sc1 nt
	global_load_dwordx4 v[150:153], v[4:5], off offset:384 sc1 nt
	global_load_dwordx4 v[138:141], v[14:15], off sc1
	global_load_dwordx4 v[146:149], v[16:17], off sc1
	global_load_dwordx4 v[134:137], v[18:19], off sc1
	s_mov_b32 s0, 0x1e000
	v_add_co_u32_e64 v8, s[0:1], s0, v6
	s_nop 1
	v_addc_co_u32_e64 v9, s[0:1], 0, v7, s[0:1]
	global_load_dwordx4 v[130:133], v[8:9], off sc1
	s_waitcnt lgkmcnt(0)
	s_barrier
	v_lshl_add_u32 v218, v206, 6, 0
	v_add_u32_e32 v217, v218, v210
	ds_read_b128 v[198:201], v216 offset:8192
	ds_read_b128 v[194:197], v216 offset:10240
	ds_read_b128 v[190:193], v216 offset:12288
	ds_read_b128 v[178:181], v216 offset:14336
	ds_read_b128 v[186:189], v217
	ds_read_b128 v[182:185], v217 offset:2048
	v_and_b32_e32 v20, 7, v0
	v_lshl_or_b32 v2, v20, 4, v2
	s_mov_b64 s[0:1], 0x2e000
	v_lshlrev_b32_e32 v212, 4, v1
	v_lshl_add_u64 v[202:203], v[6:7], 0, s[0:1]
	s_mov_b64 s[0:1], 0x290
	v_lshl_add_u64 v[4:5], s[24:25], 0, v[2:3]
	v_lshl_add_u64 v[204:205], v[4:5], 0, s[0:1]
	v_lshl_add_u64 v[252:253], v[204:205], 0, s[46:47]
	s_mov_b64 s[24:25], 0x10000
	v_mov_b32_e32 v2, v3
	v_mov_b32_e32 v4, v3
	v_mov_b32_e32 v5, v3
	v_mov_b32_e32 v6, v3
	v_mov_b32_e32 v7, v3
	v_mov_b32_e32 v8, v3
	v_mov_b32_e32 v9, v3
	v_mov_b32_e32 v10, v3
	v_mov_b32_e32 v11, v3
	v_mov_b32_e32 v12, v3
	v_mov_b32_e32 v13, v3
	v_mov_b32_e32 v14, v3
	v_mov_b32_e32 v15, v3
	v_mov_b32_e32 v16, v3
	v_mov_b32_e32 v17, v3
	v_mov_b32_e32 v18, v3
	v_mov_b32_e32 v19, v3
	v_mov_b32_e32 v20, v3
	v_and_b32_e32 v1, 63, v0
	v_add_u32_e32 v215, v211, v212
	v_add_u32_e32 v214, v218, v212
